# v12
# speedup vs baseline: 1.0486x; 1.0486x over previous
.LBB3_86:
	s_and_b64 vcc, exec, s[0:1]
	s_cbranch_vccz .LBB3_222
	v_ashrrev_i32_e32 v10, 3, v189
	v_add_u32_e32 v10, s22, v10
	v_min_i32_e32 v10, 0xc34f, v10
	v_and_b32_e32 v11, 7, v189
	v_lshl_or_b32 v176, v10, 3, v11
	v_lshl_add_u64 v[10:11], v[176:177], 2, s[62:63]
	global_load_dword v227, v[10:11], off
	v_ashrrev_i32_e32 v0, 1, v189
	v_cmp_gt_i32_e64 s[6:7], s23, v0
	v_mov_b32_e32 v5, 0
	v_mov_b32_e32 v9, 0
	s_and_saveexec_b64 s[0:1], s[6:7]
	s_cbranch_execz .LBB3_89
	v_add_u32_e32 v2, s78, v0
	v_ashrrev_i32_e32 v3, 31, v2
	v_lshl_add_u64 v[2:3], v[2:3], 2, s[58:59]
	global_load_dword v9, v[2:3], off

.LBB3_95:
	s_or_b64 exec, exec, s[4:5]
	v_and_b32_e32 v8, 1, v189
	v_cmp_eq_u32_e64 s[4:5], 0, v8
	v_lshl_add_u32 v1, v8, 4, s88
	s_waitcnt vmcnt(0)
	v_lshl_or_b32 v176, v9, 1, v8
	v_lshl_add_u64 v[10:11], v[176:177], 4, s[60:61]
	global_load_dwordx4 v[12:15], v[10:11], off
	v_lshl_or_b32 v176, v5, 1, v8
	v_lshl_add_u64 v[10:11], v[176:177], 4, s[60:61]
	global_load_dwordx4 v[16:19], v[10:11], off
	v_lshl_or_b32 v176, v7, 1, v8
	v_lshl_add_u64 v[10:11], v[176:177], 4, s[60:61]
	global_load_dwordx4 v[20:23], v[10:11], off
	v_lshl_or_b32 v176, v2, 1, v8
	v_lshl_add_u64 v[10:11], v[176:177], 4, s[60:61]
	global_load_dwordx4 v[24:27], v[10:11], off
	v_lshl_add_u32 v10, v0, 2, s90
	v_lshl_add_u32 v11, v0, 5, v1
	s_and_b64 exec, s[6:7], s[4:5]
	ds_write_b32 v10, v9
	s_and_b64 exec, s[8:9], s[4:5]
	ds_write_b32 v10, v5 offset:128
	s_and_b64 exec, s[0:1], s[4:5]
	ds_write_b32 v10, v7 offset:256
	s_and_b64 exec, vcc, s[4:5]
	ds_write_b32 v10, v2 offset:384
	s_mov_b64 exec, s[6:7]
	s_waitcnt vmcnt(3)
	ds_write_b128 v11, v[12:15]
	s_mov_b64 exec, s[8:9]
	s_waitcnt vmcnt(2)
	ds_write_b128 v11, v[16:19] offset:1024
	s_mov_b64 exec, s[0:1]
	s_waitcnt vmcnt(1)
	ds_write_b128 v11, v[20:23] offset:2048
	s_mov_b64 exec, vcc
	s_waitcnt vmcnt(0)
	ds_write_b128 v11, v[24:27] offset:3072
	s_mov_b64 exec, -1
	s_mov_b64 s[0:1], 0

.LBB3_129:
	v_mov_b32_e32 v162, v227
	v_subrev_u32_e32 v164, s78, v160
	v_lshl_add_u32 v171, v193, 2, s88
	v_min_i32_e32 v173, 0x7a, v164
	v_lshl_add_u32 v195, v173, 5, v171
	v_min_i32_e32 v173, 0x79, v164
	v_lshl_add_u32 v196, v173, 5, v171
	v_min_i32_e32 v173, 0x78, v164
	v_min_i32_e32 v199, 0x72, v164
	v_min_i32_e32 v163, 0x7e, v164
	v_min_i32_e32 v170, 0x7c, v164
	v_lshl_add_u32 v197, v173, 5, v171
	v_min_i32_e32 v173, 0x77, v164
	v_lshl_add_u32 v203, v199, 5, v171
	v_min_i32_e32 v199, 0x71, v164
	v_lshl_add_u32 v163, v163, 5, v171
	v_min_i32_e32 v166, 0x7d, v164
	v_lshl_add_u32 v170, v170, 5, v171
	v_min_i32_e32 v172, 0x7b, v164
	v_lshl_add_u32 v198, v173, 5, v171
	v_lshl_add_u32 v204, v199, 5, v171
	v_min_i32_e32 v199, 0x70, v164
	v_lshl_add_u32 v166, v166, 5, v171
	v_lshl_add_u32 v172, v172, 5, v171
	ds_read_b32 v173, v163 offset:32
	ds_read_b32 v174, v166 offset:64
	ds_read_b32 v175, v170 offset:96
	ds_read_b32 v176, v172 offset:128
	ds_read_b32 v195, v195 offset:160
	ds_read_b32 v196, v196 offset:192
	ds_read_b32 v197, v197 offset:224
	ds_read_b32 v198, v198 offset:256
	v_min_i32_e32 v163, 0x76, v164
	v_min_i32_e32 v170, 0x74, v164
	v_lshl_add_u32 v205, v199, 5, v171
	v_min_i32_e32 v199, 0x6f, v164
	v_lshl_add_u32 v163, v163, 5, v171
	v_min_i32_e32 v166, 0x75, v164
	v_lshl_add_u32 v170, v170, 5, v171
	v_min_i32_e32 v172, 0x73, v164
	v_lshl_add_u32 v206, v199, 5, v171
	v_min_i32_e32 v207, 0x6a, v164
	v_lshl_add_u32 v166, v166, 5, v171
	v_lshl_add_u32 v172, v172, 5, v171
	ds_read_b32 v199, v163 offset:288
	ds_read_b32 v200, v166 offset:320
	ds_read_b32 v201, v170 offset:352
	ds_read_b32 v202, v172 offset:384
	ds_read_b32 v203, v203 offset:416
	ds_read_b32 v204, v204 offset:448
	ds_read_b32 v205, v205 offset:480
	ds_read_b32 v206, v206 offset:512
	v_min_i32_e32 v163, 0x6e, v164
	v_min_i32_e32 v170, 0x6c, v164
	v_lshl_add_u32 v211, v207, 5, v171
	v_min_i32_e32 v207, 0x69, v164
	v_lshl_add_u32 v163, v163, 5, v171
	v_min_i32_e32 v166, 0x6d, v164
	v_lshl_add_u32 v170, v170, 5, v171
	v_min_i32_e32 v172, 0x6b, v164
	v_lshl_add_u32 v212, v207, 5, v171
	v_min_i32_e32 v207, 0x68, v164
	v_lshl_add_u32 v166, v166, 5, v171
	v_lshl_add_u32 v172, v172, 5, v171
	v_lshl_add_u32 v213, v207, 5, v171
	ds_read_b32 v207, v163 offset:544
	ds_read_b32 v208, v166 offset:576
	ds_read_b32 v209, v170 offset:608
	ds_read_b32 v210, v172 offset:640
	ds_read_b32 v211, v211 offset:672
	ds_read_b32 v170, v212 offset:704
	ds_read_b32 v163, v213 offset:736
	v_sub_u32_e32 v166, v161, v160
	v_cmp_lt_i32_e64 s[44:45], 0, v166
	v_mov_b32_e32 v172, 0xff800000
	s_and_saveexec_b64 s[0:1], s[44:45]
	s_cbranch_execz .LBB3_131
	v_min_i32_e32 v161, 0x7f, v164
	v_lshl_add_u32 v161, v161, 5, v171
	ds_read_b32 v161, v161
	s_waitcnt lgkmcnt(0)
	v_add_f32_e32 v161, v162, v161
	v_mul_f32_e32 v172, 0x3e4ccccd, v161
	v_cmp_le_f32_e32 vcc, 0, v161
	s_nop 1
	v_cndmask_b32_e32 v172, v172, v161, vcc
.LBB3_131:
	s_or_b64 exec, exec, s[0:1]
	s_waitcnt lgkmcnt(14)
	v_add_f32_e32 v161, v162, v173
	v_mul_f32_e32 v173, 0x3e4ccccd, v161
	v_cmp_le_f32_e32 vcc, 0, v161
	v_add_f32_e32 v174, v162, v174
	v_mul_f32_e32 v212, 0x3e4ccccd, v174
	v_cndmask_b32_e32 v161, v173, v161, vcc
	v_cmp_le_f32_e32 vcc, 0, v174
	v_add_f32_e32 v175, v162, v175
	v_add_f32_e32 v176, v162, v176
	v_cndmask_b32_e32 v174, v212, v174, vcc
	v_mul_f32_e32 v212, 0x3e4ccccd, v175
	v_cmp_le_f32_e32 vcc, 0, v175
	v_add_f32_e32 v195, v162, v195
	v_add_f32_e32 v196, v162, v196
	v_cndmask_b32_e32 v175, v212, v175, vcc
	v_mul_f32_e32 v212, 0x3e4ccccd, v176
	v_cmp_le_f32_e32 vcc, 0, v176
	v_add_f32_e32 v197, v162, v197
	v_add_f32_e32 v198, v162, v198
	v_cndmask_b32_e32 v176, v212, v176, vcc
	v_mul_f32_e32 v212, 0x3e4ccccd, v195
	v_cmp_le_f32_e32 vcc, 0, v195
	v_add_f32_e32 v199, v162, v199
	s_waitcnt lgkmcnt(13)
	v_add_f32_e32 v200, v162, v200
	v_cndmask_b32_e32 v195, v212, v195, vcc
	v_mul_f32_e32 v212, 0x3e4ccccd, v196
	v_cmp_le_f32_e32 vcc, 0, v196
	s_waitcnt lgkmcnt(12)
	v_add_f32_e32 v201, v162, v201
	s_waitcnt lgkmcnt(11)
	v_add_f32_e32 v202, v162, v202
	v_cndmask_b32_e32 v196, v212, v196, vcc
	v_mul_f32_e32 v212, 0x3e4ccccd, v197
	v_cmp_le_f32_e32 vcc, 0, v197
	s_waitcnt lgkmcnt(10)
	v_add_f32_e32 v203, v162, v203
	s_waitcnt lgkmcnt(9)
	v_add_f32_e32 v204, v162, v204
	v_cndmask_b32_e32 v197, v212, v197, vcc
	v_mul_f32_e32 v212, 0x3e4ccccd, v198
	v_cmp_le_f32_e32 vcc, 0, v198
	v_cmp_lt_i32_e64 s[50:51], 1, v166
	s_waitcnt lgkmcnt(8)
	v_add_f32_e32 v205, v162, v205
	v_cndmask_b32_e32 v198, v212, v198, vcc
	v_mul_f32_e32 v212, 0x3e4ccccd, v199
	v_cmp_le_f32_e32 vcc, 0, v199
	v_cndmask_b32_e64 v173, v181, v161, s[50:51]
	v_cmp_lt_i32_e64 s[48:49], 2, v166
	v_cndmask_b32_e32 v199, v212, v199, vcc
	v_mul_f32_e32 v212, 0x3e4ccccd, v200
	v_cmp_le_f32_e32 vcc, 0, v200
	v_cmp_lt_i32_e64 s[46:47], 3, v166
	s_waitcnt lgkmcnt(7)
	v_add_f32_e32 v206, v162, v206
	v_cndmask_b32_e32 v200, v212, v200, vcc
	v_mul_f32_e32 v212, 0x3e4ccccd, v201
	v_cmp_le_f32_e32 vcc, 0, v201
	v_max3_f32 v161, v172, s91, v173
	v_cndmask_b32_e64 v174, v181, v174, s[48:49]
	v_cndmask_b32_e32 v201, v212, v201, vcc
	v_mul_f32_e32 v212, 0x3e4ccccd, v202
	v_cmp_le_f32_e32 vcc, 0, v202
	v_cndmask_b32_e64 v175, v181, v175, s[46:47]
	v_cmp_lt_i32_e64 s[42:43], 4, v166
	v_cndmask_b32_e32 v202, v212, v202, vcc
	v_mul_f32_e32 v212, 0x3e4ccccd, v203
	v_cmp_le_f32_e32 vcc, 0, v203
	v_cmp_lt_i32_e64 s[40:41], 5, v166
	s_waitcnt lgkmcnt(6)
	v_add_f32_e32 v207, v162, v207
	v_cndmask_b32_e32 v203, v212, v203, vcc
	v_mul_f32_e32 v212, 0x3e4ccccd, v204
	v_cmp_le_f32_e32 vcc, 0, v204
	v_max3_f32 v161, v161, v174, v175
	v_cndmask_b32_e64 v176, v181, v176, s[42:43]
	v_cndmask_b32_e32 v204, v212, v204, vcc
	v_mul_f32_e32 v212, 0x3e4ccccd, v205
	v_cmp_le_f32_e32 vcc, 0, v205
	v_cndmask_b32_e64 v195, v181, v195, s[40:41]
	v_cmp_lt_i32_e64 s[38:39], 6, v166
	v_cndmask_b32_e32 v205, v212, v205, vcc
	v_mul_f32_e32 v212, 0x3e4ccccd, v206
	v_cmp_le_f32_e32 vcc, 0, v206
	v_cmp_lt_i32_e64 s[36:37], 7, v166
	s_waitcnt lgkmcnt(5)
	v_add_f32_e32 v208, v162, v208
	v_cndmask_b32_e32 v206, v212, v206, vcc
	v_mul_f32_e32 v212, 0x3e4ccccd, v207
	v_cmp_le_f32_e32 vcc, 0, v207
	v_max3_f32 v161, v161, v176, v195
	v_cndmask_b32_e64 v196, v181, v196, s[38:39]
	v_cndmask_b32_e64 v197, v181, v197, s[36:37]
	v_cmp_lt_i32_e64 s[34:35], 8, v166
	v_cmp_lt_i32_e64 s[30:31], 9, v166
	v_cndmask_b32_e32 v207, v212, v207, vcc
	v_mul_f32_e32 v212, 0x3e4ccccd, v208
	v_cmp_le_f32_e32 vcc, 0, v208
	s_waitcnt lgkmcnt(4)
	v_add_f32_e32 v209, v162, v209
	v_max3_f32 v161, v161, v196, v197
	v_cndmask_b32_e64 v198, v181, v198, s[34:35]
	v_cndmask_b32_e64 v199, v181, v199, s[30:31]
	v_cmp_lt_i32_e64 s[28:29], 10, v166
	v_cmp_lt_i32_e64 s[26:27], 11, v166
	v_cndmask_b32_e32 v208, v212, v208, vcc
	v_mul_f32_e32 v212, 0x3e4ccccd, v209
	v_cmp_le_f32_e32 vcc, 0, v209
	s_waitcnt lgkmcnt(3)
	v_add_f32_e32 v210, v162, v210
	v_max3_f32 v161, v161, v198, v199
	v_cndmask_b32_e64 v200, v181, v200, s[28:29]
	v_cndmask_b32_e64 v201, v181, v201, s[26:27]
	v_cmp_lt_i32_e64 s[24:25], 12, v166
	v_cmp_lt_i32_e64 s[22:23], 13, v166
	v_cndmask_b32_e32 v209, v212, v209, vcc
	v_mul_f32_e32 v212, 0x3e4ccccd, v210
	v_cmp_le_f32_e32 vcc, 0, v210
	s_waitcnt lgkmcnt(2)
	v_add_f32_e32 v211, v162, v211
	v_max3_f32 v161, v161, v200, v201
	v_cndmask_b32_e64 v202, v181, v202, s[24:25]
	v_cndmask_b32_e64 v203, v181, v203, s[22:23]
	v_cmp_lt_i32_e64 s[20:21], 14, v166
	v_cmp_lt_i32_e64 s[18:19], 15, v166
	v_cndmask_b32_e32 v210, v212, v210, vcc
	v_mul_f32_e32 v212, 0x3e4ccccd, v211
	v_cmp_le_f32_e32 vcc, 0, v211
	s_waitcnt lgkmcnt(1)
	v_add_f32_e32 v170, v162, v170
	v_max3_f32 v161, v161, v202, v203
	v_cndmask_b32_e64 v204, v181, v204, s[20:21]
	v_cndmask_b32_e64 v205, v181, v205, s[18:19]
	v_cmp_lt_i32_e64 s[16:17], 16, v166
	v_cmp_lt_i32_e64 s[14:15], 17, v166
	v_cndmask_b32_e32 v211, v212, v211, vcc
	v_mul_f32_e32 v212, 0x3e4ccccd, v170
	v_cmp_le_f32_e32 vcc, 0, v170
	v_max3_f32 v161, v161, v204, v205
	v_cndmask_b32_e64 v206, v181, v206, s[16:17]
	v_cndmask_b32_e64 v207, v181, v207, s[14:15]
	v_cmp_lt_i32_e64 s[12:13], 18, v166
	v_cmp_lt_i32_e64 s[10:11], 19, v166
	v_cndmask_b32_e32 v170, v212, v170, vcc
	v_cmp_lt_i32_e64 s[4:5], 22, v166
	s_waitcnt lgkmcnt(0)
	v_add_f32_e32 v163, v162, v163
	v_max3_f32 v161, v161, v206, v207
	v_cndmask_b32_e64 v208, v181, v208, s[12:13]
	v_cndmask_b32_e64 v209, v181, v209, s[10:11]
	v_cmp_lt_i32_e64 s[8:9], 20, v166
	v_cmp_lt_i32_e64 s[6:7], 21, v166
	v_cndmask_b32_e64 v212, v181, v170, s[4:5]
	v_mul_f32_e32 v170, 0x3e4ccccd, v163
	v_cmp_le_f32_e32 vcc, 0, v163
	v_max3_f32 v161, v161, v208, v209
	v_cndmask_b32_e64 v210, v181, v210, s[8:9]
	v_cndmask_b32_e64 v211, v181, v211, s[6:7]
	v_cndmask_b32_e32 v163, v170, v163, vcc
	v_cmp_lt_i32_e64 s[52:53], 23, v166
	v_max3_f32 v161, v161, v210, v211
	v_cmp_lt_i32_e64 s[0:1], 24, v166
	v_cndmask_b32_e64 v213, v181, v163, s[52:53]
	v_max3_f32 v170, v161, v212, v213
	s_and_saveexec_b64 s[70:71], s[0:1]
	s_cbranch_execz .LBB3_141
	v_subrev_u32_e32 v214, 24, v166
	v_mov_b32_e32 v161, 24
	v_cmp_lt_u32_e32 vcc, 1, v214
	s_mov_b64 s[82:83], -1
	s_and_saveexec_b64 s[80:81], vcc
	s_cbranch_execz .LBB3_136
	s_mov_b32 s92, s3
	s_mov_b32 s3, s66
	s_mov_b32 s67, s65
	s_mov_b32 s66, s64
	s_mov_b64 s[64:65], s[76:77]
	v_and_b32_e32 v215, -2, v214
	v_mov_b32_e32 v161, v164
	v_mov_b32_e32 v163, v162
	s_mov_b32 s69, 25
	s_mov_b32 s94, 24
	s_mov_b32 s89, 2
	s_mov_b64 s[84:85], 0
	v_mov_b32_e32 v218, v170

.LBB3_196:
	s_or_b64 exec, exec, s[4:5]
	v_lshlrev_b32_e32 v197, 7, v167
	v_add_u32_e32 v160, s88, v197
	v_lshlrev_b32_e32 v164, 4, v193
	v_add_u32_e32 v198, v160, v164
	s_waitcnt vmcnt(0)
	ds_write_b128 v198, v[20:23]
	v_mov_b32_e32 v20, s87
	ds_read_b32 v20, v20 offset:16
	s_cmp_gt_i32 s97, 0
	ds_write_b128 v198, v[16:19] offset:1024
	ds_write_b128 v198, v[28:31] offset:2048
	ds_write_b128 v198, v[24:27] offset:3072
	s_waitcnt lgkmcnt(3)
	v_add_u32_e32 v160, v194, v20
	s_cbranch_scc0 .LBB3_198
	v_min_i32_e32 v16, s79, v160
	v_lshl_add_u32 v16, v16, 2, s90
	ds_read_b32 v16, v16
	s_waitcnt lgkmcnt(0)
	v_lshl_or_b32 v176, v16, 3, v193
	v_lshl_add_u64 v[16:17], v[176:177], 4, s[72:73]
	global_load_dwordx4 v[16:19], v[16:17], off
	s_branch .LBB3_199

	.amdhsa_kernel _Z8k_layer1PKiS0_PKfS2_PK15HIP_vector_typeIjLj4EEPKDv8_DF16_S9_S2_S2_S2_PDF16_PfSB_
		.amdhsa_group_segment_fixed_size 54208
		.amdhsa_private_segment_fixed_size 0
		.amdhsa_kernarg_size 360
		.amdhsa_user_sgpr_count 2
		.amdhsa_user_sgpr_dispatch_ptr 0
		.amdhsa_user_sgpr_queue_ptr 0
		.amdhsa_user_sgpr_kernarg_segment_ptr 1
		.amdhsa_user_sgpr_dispatch_id 0
		.amdhsa_user_sgpr_kernarg_preload_length 0
		.amdhsa_user_sgpr_kernarg_preload_offset 0
		.amdhsa_user_sgpr_private_segment_size 0
		.amdhsa_uses_dynamic_stack 0
		.amdhsa_enable_private_segment 0
		.amdhsa_system_sgpr_workgroup_id_x 1
		.amdhsa_system_sgpr_workgroup_id_y 0
		.amdhsa_system_sgpr_workgroup_id_z 0
		.amdhsa_system_sgpr_workgroup_info 0
		.amdhsa_system_vgpr_workitem_id 0
		.amdhsa_next_free_vgpr 228
		.amdhsa_next_free_sgpr 100
		.amdhsa_accum_offset 228
		.amdhsa_reserve_vcc 1
		.amdhsa_float_round_mode_32 0
		.amdhsa_float_round_mode_16_64 0
		.amdhsa_float_denorm_mode_32 3
		.amdhsa_float_denorm_mode_16_64 3
		.amdhsa_dx10_clamp 1
		.amdhsa_ieee_mode 1
		.amdhsa_fp16_overflow 0
		.amdhsa_tg_split 0
		.amdhsa_exception_fp_ieee_invalid_op 0
		.amdhsa_exception_fp_denorm_src 0
		.amdhsa_exception_fp_ieee_div_zero 0
		.amdhsa_exception_fp_ieee_overflow 0
		.amdhsa_exception_fp_ieee_underflow 0
		.amdhsa_exception_fp_ieee_inexact 0
		.amdhsa_exception_int_div_zero 0
	.end_amdhsa_kernel

_Z8k_layer2PKiS0_PKfS2_PK15HIP_vector_typeIjLj4EES2_Pf:
	s_load_dwordx2 s[4:5], s[0:1], 0x0
	s_load_dwordx8 s[8:15], s[0:1], 0x8
	s_load_dwordx2 s[6:7], s[0:1], 0x28
	s_load_dwordx2 s[16:17], s[0:1], 0x30
	v_lshrrev_b32_e32 v1, 3, v0
	v_and_b32_e32 v67, 7, v0
	v_lshl_or_b32 v49, s2, 5, v1
	v_min_i32_e32 v4, 0xc34f, v49
	v_lshlrev_b32_e32 v4, 2, v4
	v_lshlrev_b32_e32 v48, 4, v67
	s_mov_b32 s23, 0x20000
	s_mov_b32 s27, 0x20000
	s_mov_b32 s31, 0x20000
	s_mov_b32 s22, 0x61a800
	s_mov_b32 s26, 0x30d40
	s_mov_b32 s30, 0x1e8480
	s_waitcnt lgkmcnt(0)
	global_load_dwordx2 v[2:3], v4, s[4:5]
	global_load_dword v51, v4, s[12:13]
	s_mov_b32 s20, s14
	s_and_b32 s21, s15, 0xffff
	s_mov_b32 s24, s10
	s_and_b32 s25, s11, 0xffff
	s_mov_b32 s28, s8
	s_and_b32 s29, s9, 0xffff
	v_mov_b32_e32 v55, 0xfffffc
	v_mov_b32_e32 v32, 0
	v_mov_b32_e32 v33, 0
	v_mov_b32_e32 v34, 0
	v_mov_b32_e32 v35, 0
	v_mov_b32_e32 v36, 0
	v_mov_b32_e32 v37, 0
	v_mov_b32_e32 v38, 0
	v_mov_b32_e32 v39, 0
	v_mov_b32_e32 v52, 0xff800000
	v_mov_b32_e32 v53, 0
	s_mov_b32 s34, 0
	s_waitcnt vmcnt(1)
	v_sub_u32_e32 v50, v3, v2
	v_add_lshl_u32 v54, v2, v67, 2
	s_nop 0
	v_mov_b32_dpp v5, v50 row_ror:8 row_mask:0xf bank_mask:0xf
	v_max_i32_e32 v5, v5, v50
	s_nop 0
	v_readlane_b32 s36, v5, 0
	v_readlane_b32 s37, v5, 16
	v_readlane_b32 s38, v5, 32
	v_readlane_b32 s39, v5, 48
	s_max_i32 s36, s36, s37
	s_max_i32 s38, s38, s39
	s_max_i32 s33, s36, s38
	s_cmp_lt_i32 s33, 1
	s_cbranch_scc1 .Lk5_epi
.Lk5_chunk:
	v_add_u32_e32 v64, s34, v67
	v_add_u32_e32 v65, 8, v64
	v_cmp_lt_i32_e64 s[40:41], v64, v50
	v_cmp_lt_i32_e64 s[42:43], v65, v50
	s_lshl_b32 s35, s34, 2
	v_add_u32_e32 v64, s35, v54
	v_add_u32_e32 v65, 32, v64
	v_cndmask_b32_e64 v64, v55, v64, s[40:41]
	v_cndmask_b32_e64 v65, v55, v65, s[42:43]
	buffer_load_dword v66, v64, s[28:31], 0 offen
	buffer_load_dword v69, v65, s[28:31], 0 offen
	s_sub_i32 s44, s33, s34
	s_waitcnt vmcnt(0)
	v_cndmask_b32_e64 v66, v55, v66, s[40:41]
	v_cndmask_b32_e64 v69, v55, v69, s[42:43]
	v_lshlrev_b32_e32 v64, 2, v66
	v_lshlrev_b32_e32 v65, 2, v69
	v_lshlrev_b32_e32 v56, 7, v66
	v_lshlrev_b32_e32 v57, 7, v69
	ds_swizzle_b32 v0, v56 offset:24
	ds_swizzle_b32 v4, v56 offset:56
	ds_swizzle_b32 v8, v56 offset:88
	ds_swizzle_b32 v12, v56 offset:120
	ds_swizzle_b32 v16, v56 offset:152
	ds_swizzle_b32 v20, v56 offset:184
	ds_swizzle_b32 v24, v56 offset:216
	ds_swizzle_b32 v28, v56 offset:248
	buffer_load_dword v64, v64, s[24:27], 0 offen
	buffer_load_dword v65, v65, s[24:27], 0 offen
	s_waitcnt lgkmcnt(7)
	v_or_b32_e32 v0, v0, v48
	buffer_load_dwordx4 v[0:3], v0, s[20:23], 0 offen
	s_waitcnt lgkmcnt(6)
	v_or_b32_e32 v4, v4, v48
	buffer_load_dwordx4 v[4:7], v4, s[20:23], 0 offen
	s_waitcnt lgkmcnt(5)
	v_or_b32_e32 v8, v8, v48
	buffer_load_dwordx4 v[8:11], v8, s[20:23], 0 offen
	s_waitcnt lgkmcnt(4)
	v_or_b32_e32 v12, v12, v48
	buffer_load_dwordx4 v[12:15], v12, s[20:23], 0 offen
	s_waitcnt lgkmcnt(3)
	v_or_b32_e32 v16, v16, v48
	buffer_load_dwordx4 v[16:19], v16, s[20:23], 0 offen
	s_waitcnt lgkmcnt(2)
	v_or_b32_e32 v20, v20, v48
	buffer_load_dwordx4 v[20:23], v20, s[20:23], 0 offen
	s_waitcnt lgkmcnt(1)
	v_or_b32_e32 v24, v24, v48
	buffer_load_dwordx4 v[24:27], v24, s[20:23], 0 offen
	s_waitcnt lgkmcnt(0)
	v_or_b32_e32 v28, v28, v48
	buffer_load_dwordx4 v[28:31], v28, s[20:23], 0 offen
	v_mov_b32_e32 v68, 0xff800000
	s_waitcnt vmcnt(8)
	v_add_f32_e32 v64, v64, v51
	v_add_f32_e32 v65, v65, v51
	v_mul_f32_e32 v66, 0x3e4ccccd, v64
	v_mul_f32_e32 v69, 0x3e4ccccd, v65
	v_max_f32_e32 v64, v64, v66
	v_max_f32_e32 v65, v65, v69
	v_cndmask_b32_e64 v64, v68, v64, s[40:41]
	v_cndmask_b32_e64 v65, v68, v65, s[42:43]
	v_max_f32_e32 v66, v64, v65
	s_nop 1
	v_mov_b32_dpp v69, v66 quad_perm:[1,0,3,2] row_mask:0xf bank_mask:0xf bound_ctrl:1
	v_max_f32_e32 v66, v66, v69
	s_nop 1
	v_mov_b32_dpp v69, v66 quad_perm:[2,3,0,1] row_mask:0xf bank_mask:0xf bound_ctrl:1
	v_max_f32_e32 v66, v66, v69
	s_nop 1
	v_mov_b32_dpp v69, v66 row_half_mirror row_mask:0xf bank_mask:0xf bound_ctrl:1
	v_max3_f32 v66, v52, v66, v69
	v_sub_f32_e32 v62, v52, v66
	v_sub_f32_e32 v64, v64, v66
	v_sub_f32_e32 v65, v65, v66
	v_mul_f32_e32 v62, 0x3fb8aa3b, v62
	v_mul_f32_e32 v64, 0x3fb8aa3b, v64
	v_mul_f32_e32 v65, 0x3fb8aa3b, v65
	v_exp_f32_e32 v62, v62
	v_exp_f32_e32 v64, v64
	v_exp_f32_e32 v65, v65
	v_cmp_neq_f32_e32 vcc, 0xff800000, v66
	v_mov_b32_e32 v52, v66
	v_cndmask_b32_e64 v58, 0, v64, s[40:41]
	v_cndmask_b32_e64 v59, 0, v65, s[42:43]
	v_cndmask_b32_e32 v62, 1.0, v62, vcc
	ds_swizzle_b32 v40, v58 offset:24
	ds_swizzle_b32 v41, v58 offset:56
	ds_swizzle_b32 v42, v58 offset:88
	ds_swizzle_b32 v43, v58 offset:120
	ds_swizzle_b32 v44, v58 offset:152
	ds_swizzle_b32 v45, v58 offset:184
	ds_swizzle_b32 v46, v58 offset:216
	ds_swizzle_b32 v47, v58 offset:248
	v_add_f32_e32 v69, v58, v59
	v_pk_mul_f32 v[32:33], v[62:63], v[32:33] op_sel_hi:[0,1]
	v_pk_mul_f32 v[34:35], v[62:63], v[34:35] op_sel_hi:[0,1]
	v_add_f32_dpp v69, v69, v69 quad_perm:[1,0,3,2] row_mask:0xf bank_mask:0xf bound_ctrl:1
	v_pk_mul_f32 v[36:37], v[62:63], v[36:37] op_sel_hi:[0,1]
	v_pk_mul_f32 v[38:39], v[62:63], v[38:39] op_sel_hi:[0,1]
	v_add_f32_dpp v69, v69, v69 quad_perm:[2,3,0,1] row_mask:0xf bank_mask:0xf bound_ctrl:1
	s_nop 1
	v_mov_b32_dpp v66, v69 row_half_mirror row_mask:0xf bank_mask:0xf bound_ctrl:1
	v_add_f32_e32 v69, v69, v66
	v_fma_f32 v53, v53, v62, v69
	s_cmp_lt_i32 s44, 9
	s_cbranch_scc1 .Lk5_half
	ds_swizzle_b32 v60, v57 offset:24
	ds_swizzle_b32 v61, v57 offset:56
	s_waitcnt vmcnt(7)
	s_waitcnt lgkmcnt(1)
	v_fma_mix_f32 v32, v40, v0, v32 op_sel_hi:[0,1,0]
	v_fma_mix_f32 v33, v40, v0, v33 op_sel:[0,1,0] op_sel_hi:[0,1,0]
	v_fma_mix_f32 v34, v40, v1, v34 op_sel_hi:[0,1,0]
	v_fma_mix_f32 v35, v40, v1, v35 op_sel:[0,1,0] op_sel_hi:[0,1,0]
	v_fma_mix_f32 v36, v40, v2, v36 op_sel_hi:[0,1,0]
	v_fma_mix_f32 v37, v40, v2, v37 op_sel:[0,1,0] op_sel_hi:[0,1,0]
	v_fma_mix_f32 v38, v40, v3, v38 op_sel_hi:[0,1,0]
	v_fma_mix_f32 v39, v40, v3, v39 op_sel:[0,1,0] op_sel_hi:[0,1,0]
	v_or_b32_e32 v60, v60, v48
	buffer_load_dwordx4 v[0:3], v60, s[20:23], 0 offen
	ds_swizzle_b32 v60, v57 offset:88
	s_waitcnt vmcnt(7)
	s_waitcnt lgkmcnt(1)
	v_fma_mix_f32 v32, v41, v4, v32 op_sel_hi:[0,1,0]
	v_fma_mix_f32 v33, v41, v4, v33 op_sel:[0,1,0] op_sel_hi:[0,1,0]
	v_fma_mix_f32 v34, v41, v5, v34 op_sel_hi:[0,1,0]
	v_fma_mix_f32 v35, v41, v5, v35 op_sel:[0,1,0] op_sel_hi:[0,1,0]
	v_fma_mix_f32 v36, v41, v6, v36 op_sel_hi:[0,1,0]
	v_fma_mix_f32 v37, v41, v6, v37 op_sel:[0,1,0] op_sel_hi:[0,1,0]
	v_fma_mix_f32 v38, v41, v7, v38 op_sel_hi:[0,1,0]
	v_fma_mix_f32 v39, v41, v7, v39 op_sel:[0,1,0] op_sel_hi:[0,1,0]
	v_or_b32_e32 v61, v61, v48
	buffer_load_dwordx4 v[4:7], v61, s[20:23], 0 offen
	ds_swizzle_b32 v61, v57 offset:120
	s_waitcnt vmcnt(7)
	s_waitcnt lgkmcnt(1)
	v_fma_mix_f32 v32, v42, v8, v32 op_sel_hi:[0,1,0]
	v_fma_mix_f32 v33, v42, v8, v33 op_sel:[0,1,0] op_sel_hi:[0,1,0]
	v_fma_mix_f32 v34, v42, v9, v34 op_sel_hi:[0,1,0]
	v_fma_mix_f32 v35, v42, v9, v35 op_sel:[0,1,0] op_sel_hi:[0,1,0]
	v_fma_mix_f32 v36, v42, v10, v36 op_sel_hi:[0,1,0]
	v_fma_mix_f32 v37, v42, v10, v37 op_sel:[0,1,0] op_sel_hi:[0,1,0]
	v_fma_mix_f32 v38, v42, v11, v38 op_sel_hi:[0,1,0]
	v_fma_mix_f32 v39, v42, v11, v39 op_sel:[0,1,0] op_sel_hi:[0,1,0]
	v_or_b32_e32 v60, v60, v48
	buffer_load_dwordx4 v[8:11], v60, s[20:23], 0 offen
	ds_swizzle_b32 v60, v57 offset:152
	s_waitcnt vmcnt(7)
	s_waitcnt lgkmcnt(1)
	v_fma_mix_f32 v32, v43, v12, v32 op_sel_hi:[0,1,0]
	v_fma_mix_f32 v33, v43, v12, v33 op_sel:[0,1,0] op_sel_hi:[0,1,0]
	v_fma_mix_f32 v34, v43, v13, v34 op_sel_hi:[0,1,0]
	v_fma_mix_f32 v35, v43, v13, v35 op_sel:[0,1,0] op_sel_hi:[0,1,0]
	v_fma_mix_f32 v36, v43, v14, v36 op_sel_hi:[0,1,0]
	v_fma_mix_f32 v37, v43, v14, v37 op_sel:[0,1,0] op_sel_hi:[0,1,0]
	v_fma_mix_f32 v38, v43, v15, v38 op_sel_hi:[0,1,0]
	v_fma_mix_f32 v39, v43, v15, v39 op_sel:[0,1,0] op_sel_hi:[0,1,0]
	v_or_b32_e32 v61, v61, v48
	buffer_load_dwordx4 v[12:15], v61, s[20:23], 0 offen
	ds_swizzle_b32 v61, v57 offset:184
	s_waitcnt vmcnt(7)
	s_waitcnt lgkmcnt(1)
	v_fma_mix_f32 v32, v44, v16, v32 op_sel_hi:[0,1,0]
	v_fma_mix_f32 v33, v44, v16, v33 op_sel:[0,1,0] op_sel_hi:[0,1,0]
	v_fma_mix_f32 v34, v44, v17, v34 op_sel_hi:[0,1,0]
	v_fma_mix_f32 v35, v44, v17, v35 op_sel:[0,1,0] op_sel_hi:[0,1,0]
	v_fma_mix_f32 v36, v44, v18, v36 op_sel_hi:[0,1,0]
	v_fma_mix_f32 v37, v44, v18, v37 op_sel:[0,1,0] op_sel_hi:[0,1,0]
	v_fma_mix_f32 v38, v44, v19, v38 op_sel_hi:[0,1,0]
	v_fma_mix_f32 v39, v44, v19, v39 op_sel:[0,1,0] op_sel_hi:[0,1,0]
	v_or_b32_e32 v60, v60, v48
	buffer_load_dwordx4 v[16:19], v60, s[20:23], 0 offen
	ds_swizzle_b32 v60, v57 offset:216
	s_waitcnt vmcnt(7)
	s_waitcnt lgkmcnt(1)
	v_fma_mix_f32 v32, v45, v20, v32 op_sel_hi:[0,1,0]
	v_fma_mix_f32 v33, v45, v20, v33 op_sel:[0,1,0] op_sel_hi:[0,1,0]
	v_fma_mix_f32 v34, v45, v21, v34 op_sel_hi:[0,1,0]
	v_fma_mix_f32 v35, v45, v21, v35 op_sel:[0,1,0] op_sel_hi:[0,1,0]
	v_fma_mix_f32 v36, v45, v22, v36 op_sel_hi:[0,1,0]
	v_fma_mix_f32 v37, v45, v22, v37 op_sel:[0,1,0] op_sel_hi:[0,1,0]
	v_fma_mix_f32 v38, v45, v23, v38 op_sel_hi:[0,1,0]
	v_fma_mix_f32 v39, v45, v23, v39 op_sel:[0,1,0] op_sel_hi:[0,1,0]
	v_or_b32_e32 v61, v61, v48
	buffer_load_dwordx4 v[20:23], v61, s[20:23], 0 offen
	ds_swizzle_b32 v61, v57 offset:248
	s_waitcnt vmcnt(7)
	s_waitcnt lgkmcnt(1)
	v_fma_mix_f32 v32, v46, v24, v32 op_sel_hi:[0,1,0]
	v_fma_mix_f32 v33, v46, v24, v33 op_sel:[0,1,0] op_sel_hi:[0,1,0]
	v_fma_mix_f32 v34, v46, v25, v34 op_sel_hi:[0,1,0]
	v_fma_mix_f32 v35, v46, v25, v35 op_sel:[0,1,0] op_sel_hi:[0,1,0]
	v_fma_mix_f32 v36, v46, v26, v36 op_sel_hi:[0,1,0]
	v_fma_mix_f32 v37, v46, v26, v37 op_sel:[0,1,0] op_sel_hi:[0,1,0]
	v_fma_mix_f32 v38, v46, v27, v38 op_sel_hi:[0,1,0]
	v_fma_mix_f32 v39, v46, v27, v39 op_sel:[0,1,0] op_sel_hi:[0,1,0]
	v_or_b32_e32 v60, v60, v48
	buffer_load_dwordx4 v[24:27], v60, s[20:23], 0 offen
	s_waitcnt vmcnt(7)
	s_waitcnt lgkmcnt(0)
	v_fma_mix_f32 v32, v47, v28, v32 op_sel_hi:[0,1,0]
	v_fma_mix_f32 v33, v47, v28, v33 op_sel:[0,1,0] op_sel_hi:[0,1,0]
	v_fma_mix_f32 v34, v47, v29, v34 op_sel_hi:[0,1,0]
	v_fma_mix_f32 v35, v47, v29, v35 op_sel:[0,1,0] op_sel_hi:[0,1,0]
	v_fma_mix_f32 v36, v47, v30, v36 op_sel_hi:[0,1,0]
	v_fma_mix_f32 v37, v47, v30, v37 op_sel:[0,1,0] op_sel_hi:[0,1,0]
	v_fma_mix_f32 v38, v47, v31, v38 op_sel_hi:[0,1,0]
	v_fma_mix_f32 v39, v47, v31, v39 op_sel:[0,1,0] op_sel_hi:[0,1,0]
	v_or_b32_e32 v61, v61, v48
	buffer_load_dwordx4 v[28:31], v61, s[20:23], 0 offen
	ds_swizzle_b32 v40, v59 offset:24
	ds_swizzle_b32 v41, v59 offset:56
	ds_swizzle_b32 v42, v59 offset:88
	ds_swizzle_b32 v43, v59 offset:120
	ds_swizzle_b32 v44, v59 offset:152
	ds_swizzle_b32 v45, v59 offset:184
	ds_swizzle_b32 v46, v59 offset:216
	ds_swizzle_b32 v47, v59 offset:248
	s_waitcnt vmcnt(7)
	s_waitcnt lgkmcnt(7)
	v_fma_mix_f32 v32, v40, v0, v32 op_sel_hi:[0,1,0]
	v_fma_mix_f32 v33, v40, v0, v33 op_sel:[0,1,0] op_sel_hi:[0,1,0]
	v_fma_mix_f32 v34, v40, v1, v34 op_sel_hi:[0,1,0]
	v_fma_mix_f32 v35, v40, v1, v35 op_sel:[0,1,0] op_sel_hi:[0,1,0]
	v_fma_mix_f32 v36, v40, v2, v36 op_sel_hi:[0,1,0]
	v_fma_mix_f32 v37, v40, v2, v37 op_sel:[0,1,0] op_sel_hi:[0,1,0]
	v_fma_mix_f32 v38, v40, v3, v38 op_sel_hi:[0,1,0]
	v_fma_mix_f32 v39, v40, v3, v39 op_sel:[0,1,0] op_sel_hi:[0,1,0]
	s_waitcnt vmcnt(6)
	s_waitcnt lgkmcnt(6)
	v_fma_mix_f32 v32, v41, v4, v32 op_sel_hi:[0,1,0]
	v_fma_mix_f32 v33, v41, v4, v33 op_sel:[0,1,0] op_sel_hi:[0,1,0]
	v_fma_mix_f32 v34, v41, v5, v34 op_sel_hi:[0,1,0]
	v_fma_mix_f32 v35, v41, v5, v35 op_sel:[0,1,0] op_sel_hi:[0,1,0]
	v_fma_mix_f32 v36, v41, v6, v36 op_sel_hi:[0,1,0]
	v_fma_mix_f32 v37, v41, v6, v37 op_sel:[0,1,0] op_sel_hi:[0,1,0]
	v_fma_mix_f32 v38, v41, v7, v38 op_sel_hi:[0,1,0]
	v_fma_mix_f32 v39, v41, v7, v39 op_sel:[0,1,0] op_sel_hi:[0,1,0]
	s_waitcnt vmcnt(5)
	s_waitcnt lgkmcnt(5)
	v_fma_mix_f32 v32, v42, v8, v32 op_sel_hi:[0,1,0]
	v_fma_mix_f32 v33, v42, v8, v33 op_sel:[0,1,0] op_sel_hi:[0,1,0]
	v_fma_mix_f32 v34, v42, v9, v34 op_sel_hi:[0,1,0]
	v_fma_mix_f32 v35, v42, v9, v35 op_sel:[0,1,0] op_sel_hi:[0,1,0]
	v_fma_mix_f32 v36, v42, v10, v36 op_sel_hi:[0,1,0]
	v_fma_mix_f32 v37, v42, v10, v37 op_sel:[0,1,0] op_sel_hi:[0,1,0]
	v_fma_mix_f32 v38, v42, v11, v38 op_sel_hi:[0,1,0]
	v_fma_mix_f32 v39, v42, v11, v39 op_sel:[0,1,0] op_sel_hi:[0,1,0]
	s_waitcnt vmcnt(4)
	s_waitcnt lgkmcnt(4)
	v_fma_mix_f32 v32, v43, v12, v32 op_sel_hi:[0,1,0]
	v_fma_mix_f32 v33, v43, v12, v33 op_sel:[0,1,0] op_sel_hi:[0,1,0]
	v_fma_mix_f32 v34, v43, v13, v34 op_sel_hi:[0,1,0]
	v_fma_mix_f32 v35, v43, v13, v35 op_sel:[0,1,0] op_sel_hi:[0,1,0]
	v_fma_mix_f32 v36, v43, v14, v36 op_sel_hi:[0,1,0]
	v_fma_mix_f32 v37, v43, v14, v37 op_sel:[0,1,0] op_sel_hi:[0,1,0]
	v_fma_mix_f32 v38, v43, v15, v38 op_sel_hi:[0,1,0]
	v_fma_mix_f32 v39, v43, v15, v39 op_sel:[0,1,0] op_sel_hi:[0,1,0]
	s_waitcnt vmcnt(3)
	s_waitcnt lgkmcnt(3)
	v_fma_mix_f32 v32, v44, v16, v32 op_sel_hi:[0,1,0]
	v_fma_mix_f32 v33, v44, v16, v33 op_sel:[0,1,0] op_sel_hi:[0,1,0]
	v_fma_mix_f32 v34, v44, v17, v34 op_sel_hi:[0,1,0]
	v_fma_mix_f32 v35, v44, v17, v35 op_sel:[0,1,0] op_sel_hi:[0,1,0]
	v_fma_mix_f32 v36, v44, v18, v36 op_sel_hi:[0,1,0]
	v_fma_mix_f32 v37, v44, v18, v37 op_sel:[0,1,0] op_sel_hi:[0,1,0]
	v_fma_mix_f32 v38, v44, v19, v38 op_sel_hi:[0,1,0]
	v_fma_mix_f32 v39, v44, v19, v39 op_sel:[0,1,0] op_sel_hi:[0,1,0]
	s_waitcnt vmcnt(2)
	s_waitcnt lgkmcnt(2)
	v_fma_mix_f32 v32, v45, v20, v32 op_sel_hi:[0,1,0]
	v_fma_mix_f32 v33, v45, v20, v33 op_sel:[0,1,0] op_sel_hi:[0,1,0]
	v_fma_mix_f32 v34, v45, v21, v34 op_sel_hi:[0,1,0]
	v_fma_mix_f32 v35, v45, v21, v35 op_sel:[0,1,0] op_sel_hi:[0,1,0]
	v_fma_mix_f32 v36, v45, v22, v36 op_sel_hi:[0,1,0]
	v_fma_mix_f32 v37, v45, v22, v37 op_sel:[0,1,0] op_sel_hi:[0,1,0]
	v_fma_mix_f32 v38, v45, v23, v38 op_sel_hi:[0,1,0]
	v_fma_mix_f32 v39, v45, v23, v39 op_sel:[0,1,0] op_sel_hi:[0,1,0]
	s_waitcnt vmcnt(1)
	s_waitcnt lgkmcnt(1)
	v_fma_mix_f32 v32, v46, v24, v32 op_sel_hi:[0,1,0]
	v_fma_mix_f32 v33, v46, v24, v33 op_sel:[0,1,0] op_sel_hi:[0,1,0]
	v_fma_mix_f32 v34, v46, v25, v34 op_sel_hi:[0,1,0]
	v_fma_mix_f32 v35, v46, v25, v35 op_sel:[0,1,0] op_sel_hi:[0,1,0]
	v_fma_mix_f32 v36, v46, v26, v36 op_sel_hi:[0,1,0]
	v_fma_mix_f32 v37, v46, v26, v37 op_sel:[0,1,0] op_sel_hi:[0,1,0]
	v_fma_mix_f32 v38, v46, v27, v38 op_sel_hi:[0,1,0]
	v_fma_mix_f32 v39, v46, v27, v39 op_sel:[0,1,0] op_sel_hi:[0,1,0]
	s_waitcnt vmcnt(0)
	s_waitcnt lgkmcnt(0)
	v_fma_mix_f32 v32, v47, v28, v32 op_sel_hi:[0,1,0]
	v_fma_mix_f32 v33, v47, v28, v33 op_sel:[0,1,0] op_sel_hi:[0,1,0]
	v_fma_mix_f32 v34, v47, v29, v34 op_sel_hi:[0,1,0]
	v_fma_mix_f32 v35, v47, v29, v35 op_sel:[0,1,0] op_sel_hi:[0,1,0]
	v_fma_mix_f32 v36, v47, v30, v36 op_sel_hi:[0,1,0]
	v_fma_mix_f32 v37, v47, v30, v37 op_sel:[0,1,0] op_sel_hi:[0,1,0]
	v_fma_mix_f32 v38, v47, v31, v38 op_sel_hi:[0,1,0]
	v_fma_mix_f32 v39, v47, v31, v39 op_sel:[0,1,0] op_sel_hi:[0,1,0]
	s_branch .Lk5_next
.Lk5_half:
	s_waitcnt vmcnt(7)
	s_waitcnt lgkmcnt(7)
	v_fma_mix_f32 v32, v40, v0, v32 op_sel_hi:[0,1,0]
	v_fma_mix_f32 v33, v40, v0, v33 op_sel:[0,1,0] op_sel_hi:[0,1,0]
	v_fma_mix_f32 v34, v40, v1, v34 op_sel_hi:[0,1,0]
	v_fma_mix_f32 v35, v40, v1, v35 op_sel:[0,1,0] op_sel_hi:[0,1,0]
	v_fma_mix_f32 v36, v40, v2, v36 op_sel_hi:[0,1,0]
	v_fma_mix_f32 v37, v40, v2, v37 op_sel:[0,1,0] op_sel_hi:[0,1,0]
	v_fma_mix_f32 v38, v40, v3, v38 op_sel_hi:[0,1,0]
	v_fma_mix_f32 v39, v40, v3, v39 op_sel:[0,1,0] op_sel_hi:[0,1,0]
	s_waitcnt vmcnt(6)
	s_waitcnt lgkmcnt(6)
	v_fma_mix_f32 v32, v41, v4, v32 op_sel_hi:[0,1,0]
	v_fma_mix_f32 v33, v41, v4, v33 op_sel:[0,1,0] op_sel_hi:[0,1,0]
	v_fma_mix_f32 v34, v41, v5, v34 op_sel_hi:[0,1,0]
	v_fma_mix_f32 v35, v41, v5, v35 op_sel:[0,1,0] op_sel_hi:[0,1,0]
	v_fma_mix_f32 v36, v41, v6, v36 op_sel_hi:[0,1,0]
	v_fma_mix_f32 v37, v41, v6, v37 op_sel:[0,1,0] op_sel_hi:[0,1,0]
	v_fma_mix_f32 v38, v41, v7, v38 op_sel_hi:[0,1,0]
	v_fma_mix_f32 v39, v41, v7, v39 op_sel:[0,1,0] op_sel_hi:[0,1,0]
	s_waitcnt vmcnt(5)
	s_waitcnt lgkmcnt(5)
	v_fma_mix_f32 v32, v42, v8, v32 op_sel_hi:[0,1,0]
	v_fma_mix_f32 v33, v42, v8, v33 op_sel:[0,1,0] op_sel_hi:[0,1,0]
	v_fma_mix_f32 v34, v42, v9, v34 op_sel_hi:[0,1,0]
	v_fma_mix_f32 v35, v42, v9, v35 op_sel:[0,1,0] op_sel_hi:[0,1,0]
	v_fma_mix_f32 v36, v42, v10, v36 op_sel_hi:[0,1,0]
	v_fma_mix_f32 v37, v42, v10, v37 op_sel:[0,1,0] op_sel_hi:[0,1,0]
	v_fma_mix_f32 v38, v42, v11, v38 op_sel_hi:[0,1,0]
	v_fma_mix_f32 v39, v42, v11, v39 op_sel:[0,1,0] op_sel_hi:[0,1,0]
	s_waitcnt vmcnt(4)
	s_waitcnt lgkmcnt(4)
	v_fma_mix_f32 v32, v43, v12, v32 op_sel_hi:[0,1,0]
	v_fma_mix_f32 v33, v43, v12, v33 op_sel:[0,1,0] op_sel_hi:[0,1,0]
	v_fma_mix_f32 v34, v43, v13, v34 op_sel_hi:[0,1,0]
	v_fma_mix_f32 v35, v43, v13, v35 op_sel:[0,1,0] op_sel_hi:[0,1,0]
	v_fma_mix_f32 v36, v43, v14, v36 op_sel_hi:[0,1,0]
	v_fma_mix_f32 v37, v43, v14, v37 op_sel:[0,1,0] op_sel_hi:[0,1,0]
	v_fma_mix_f32 v38, v43, v15, v38 op_sel_hi:[0,1,0]
	v_fma_mix_f32 v39, v43, v15, v39 op_sel:[0,1,0] op_sel_hi:[0,1,0]
	s_waitcnt vmcnt(3)
	s_waitcnt lgkmcnt(3)
	v_fma_mix_f32 v32, v44, v16, v32 op_sel_hi:[0,1,0]
	v_fma_mix_f32 v33, v44, v16, v33 op_sel:[0,1,0] op_sel_hi:[0,1,0]
	v_fma_mix_f32 v34, v44, v17, v34 op_sel_hi:[0,1,0]
	v_fma_mix_f32 v35, v44, v17, v35 op_sel:[0,1,0] op_sel_hi:[0,1,0]
	v_fma_mix_f32 v36, v44, v18, v36 op_sel_hi:[0,1,0]
	v_fma_mix_f32 v37, v44, v18, v37 op_sel:[0,1,0] op_sel_hi:[0,1,0]
	v_fma_mix_f32 v38, v44, v19, v38 op_sel_hi:[0,1,0]
	v_fma_mix_f32 v39, v44, v19, v39 op_sel:[0,1,0] op_sel_hi:[0,1,0]
	s_waitcnt vmcnt(2)
	s_waitcnt lgkmcnt(2)
	v_fma_mix_f32 v32, v45, v20, v32 op_sel_hi:[0,1,0]
	v_fma_mix_f32 v33, v45, v20, v33 op_sel:[0,1,0] op_sel_hi:[0,1,0]
	v_fma_mix_f32 v34, v45, v21, v34 op_sel_hi:[0,1,0]
	v_fma_mix_f32 v35, v45, v21, v35 op_sel:[0,1,0] op_sel_hi:[0,1,0]
	v_fma_mix_f32 v36, v45, v22, v36 op_sel_hi:[0,1,0]
	v_fma_mix_f32 v37, v45, v22, v37 op_sel:[0,1,0] op_sel_hi:[0,1,0]
	v_fma_mix_f32 v38, v45, v23, v38 op_sel_hi:[0,1,0]
	v_fma_mix_f32 v39, v45, v23, v39 op_sel:[0,1,0] op_sel_hi:[0,1,0]
	s_waitcnt vmcnt(1)
	s_waitcnt lgkmcnt(1)
	v_fma_mix_f32 v32, v46, v24, v32 op_sel_hi:[0,1,0]
	v_fma_mix_f32 v33, v46, v24, v33 op_sel:[0,1,0] op_sel_hi:[0,1,0]
	v_fma_mix_f32 v34, v46, v25, v34 op_sel_hi:[0,1,0]
	v_fma_mix_f32 v35, v46, v25, v35 op_sel:[0,1,0] op_sel_hi:[0,1,0]
	v_fma_mix_f32 v36, v46, v26, v36 op_sel_hi:[0,1,0]
	v_fma_mix_f32 v37, v46, v26, v37 op_sel:[0,1,0] op_sel_hi:[0,1,0]
	v_fma_mix_f32 v38, v46, v27, v38 op_sel_hi:[0,1,0]
	v_fma_mix_f32 v39, v46, v27, v39 op_sel:[0,1,0] op_sel_hi:[0,1,0]
	s_waitcnt vmcnt(0)
	s_waitcnt lgkmcnt(0)
	v_fma_mix_f32 v32, v47, v28, v32 op_sel_hi:[0,1,0]
	v_fma_mix_f32 v33, v47, v28, v33 op_sel:[0,1,0] op_sel_hi:[0,1,0]
	v_fma_mix_f32 v34, v47, v29, v34 op_sel_hi:[0,1,0]
	v_fma_mix_f32 v35, v47, v29, v35 op_sel:[0,1,0] op_sel_hi:[0,1,0]
	v_fma_mix_f32 v36, v47, v30, v36 op_sel_hi:[0,1,0]
	v_fma_mix_f32 v37, v47, v30, v37 op_sel:[0,1,0] op_sel_hi:[0,1,0]
	v_fma_mix_f32 v38, v47, v31, v38 op_sel_hi:[0,1,0]
	v_fma_mix_f32 v39, v47, v31, v39 op_sel:[0,1,0] op_sel_hi:[0,1,0]
.Lk5_next:
	s_add_i32 s34, s34, 16
	s_cmp_lt_i32 s34, s33
	s_cbranch_scc1 .Lk5_chunk
.Lk5_epi:
	v_lshlrev_b32_e32 v64, 1, v48
	global_load_dwordx4 v[0:3], v64, s[6:7]
	global_load_dwordx4 v[4:7], v64, s[6:7] offset:16
	v_div_scale_f32 v65, s[2:3], v53, v53, 1.0
	v_rcp_f32_e32 v66, v65
	v_min_i32_e32 v68, 0xc34f, v49
	v_lshlrev_b32_e32 v68, 8, v68
	v_fma_f32 v62, -v65, v66, 1.0
	v_div_scale_f32 v63, vcc, 1.0, v53, 1.0
	v_fmac_f32_e32 v66, v62, v66
	v_mul_f32_e32 v62, v63, v66
	v_fma_f32 v69, -v65, v62, v63
	v_fmac_f32_e32 v62, v69, v66
	v_fma_f32 v65, -v65, v62, v63
	v_div_fmas_f32 v65, v65, v66, v62
	v_div_fixup_f32 v65, v65, v53, 1.0
	v_cmp_lt_f32_e32 vcc, 0, v53
	v_or_b32_e32 v68, v68, v64
	s_nop 0
	v_cndmask_b32_e32 v62, 0, v65, vcc
	s_waitcnt vmcnt(0)
	v_pk_fma_f32 v[32:33], v[32:33], v[62:63], v[0:1] op_sel_hi:[1,0,1]
	v_pk_fma_f32 v[34:35], v[34:35], v[62:63], v[2:3] op_sel_hi:[1,0,1]
	v_pk_fma_f32 v[36:37], v[36:37], v[62:63], v[4:5] op_sel_hi:[1,0,1]
	v_pk_fma_f32 v[38:39], v[38:39], v[62:63], v[6:7] op_sel_hi:[1,0,1]
	v_cmp_gt_i32_e32 vcc, 0xc350, v49
	s_and_saveexec_b64 s[2:3], vcc
	global_store_dwordx4 v68, v[32:35], s[16:17]
	global_store_dwordx4 v68, v[36:39], s[16:17] offset:16
	s_endpgm

	.amdhsa_kernel _Z8k_layer2PKiS0_PKfS2_PK15HIP_vector_typeIjLj4EES2_Pf
		.amdhsa_group_segment_fixed_size 0
		.amdhsa_private_segment_fixed_size 0
		.amdhsa_kernarg_size 56
		.amdhsa_user_sgpr_count 2
		.amdhsa_user_sgpr_dispatch_ptr 0
		.amdhsa_user_sgpr_queue_ptr 0
		.amdhsa_user_sgpr_kernarg_segment_ptr 1
		.amdhsa_user_sgpr_dispatch_id 0
		.amdhsa_user_sgpr_kernarg_preload_length 0
		.amdhsa_user_sgpr_kernarg_preload_offset 0
		.amdhsa_user_sgpr_private_segment_size 0
		.amdhsa_uses_dynamic_stack 0
		.amdhsa_enable_private_segment 0
		.amdhsa_system_sgpr_workgroup_id_x 1
		.amdhsa_system_sgpr_workgroup_id_y 0
		.amdhsa_system_sgpr_workgroup_id_z 0
		.amdhsa_system_sgpr_workgroup_info 0
		.amdhsa_system_vgpr_workitem_id 0
		.amdhsa_next_free_vgpr 70
		.amdhsa_next_free_sgpr 46
		.amdhsa_accum_offset 72
		.amdhsa_reserve_vcc 1
		.amdhsa_float_round_mode_32 0
		.amdhsa_float_round_mode_16_64 0
		.amdhsa_float_denorm_mode_32 3
		.amdhsa_float_denorm_mode_16_64 3
		.amdhsa_dx10_clamp 1
		.amdhsa_ieee_mode 1
		.amdhsa_fp16_overflow 0
		.amdhsa_tg_split 0
		.amdhsa_exception_fp_ieee_invalid_op 0
		.amdhsa_exception_fp_denorm_src 0
		.amdhsa_exception_fp_ieee_div_zero 0
		.amdhsa_exception_fp_ieee_overflow 0
		.amdhsa_exception_fp_ieee_underflow 0
		.amdhsa_exception_fp_ieee_inexact 0
		.amdhsa_exception_int_div_zero 0
	.end_amdhsa_kernel

amdhsa.kernels:
  - .agpr_count:     0
    .args:
      - .actual_access:  read_only
        .address_space:  global
        .offset:         0
        .size:           8
        .value_kind:     global_buffer
      - .actual_access:  read_only
        .address_space:  global
        .offset:         8
        .size:           8
        .value_kind:     global_buffer
      - .actual_access:  read_only
        .address_space:  global
        .offset:         16
        .size:           8
        .value_kind:     global_buffer
      - .actual_access:  read_only
        .address_space:  global
        .offset:         24
        .size:           8
        .value_kind:     global_buffer
      - .actual_access:  read_only
        .address_space:  global
        .offset:         32
        .size:           8
        .value_kind:     global_buffer
      - .actual_access:  write_only
        .address_space:  global
        .offset:         40
        .size:           8
        .value_kind:     global_buffer
      - .actual_access:  write_only
        .address_space:  global
        .offset:         48
        .size:           8
        .value_kind:     global_buffer
      - .actual_access:  write_only
        .address_space:  global
        .offset:         56
        .size:           8
        .value_kind:     global_buffer
      - .actual_access:  write_only
        .address_space:  global
        .offset:         64
        .size:           8
        .value_kind:     global_buffer
    .group_segment_fixed_size: 1024
    .kernarg_segment_align: 8
    .kernarg_segment_size: 72
    .language:       OpenCL C
    .language_version:
      - 2
      - 0
    .max_flat_workgroup_size: 512
    .name:           _Z11k_hist_prepPKiPKfS2_S2_S2_PiPfPDF16_S5_
    .private_segment_fixed_size: 0
    .sgpr_count:     20
    .sgpr_spill_count: 0
    .symbol:         _Z11k_hist_prepPKiPKfS2_S2_S2_PiPfPDF16_S5_.kd
    .uniform_work_group_size: 1
    .uses_dynamic_stack: false
    .vgpr_count:     42
    .vgpr_spill_count: 0
    .wavefront_size: 64
  - .agpr_count:     0
    .args:
      - .actual_access:  read_only
        .address_space:  global
        .offset:         0
        .size:           8
        .value_kind:     global_buffer
      - .actual_access:  read_only
        .address_space:  global
        .offset:         8
        .size:           8
        .value_kind:     global_buffer
      - .actual_access:  write_only
        .address_space:  global
        .offset:         16
        .size:           8
        .value_kind:     global_buffer
      - .actual_access:  write_only
        .address_space:  global
        .offset:         24
        .size:           8
        .value_kind:     global_buffer
      - .actual_access:  read_only
        .address_space:  global
        .offset:         32
        .size:           8
        .value_kind:     global_buffer
      - .actual_access:  read_only
        .address_space:  global
        .offset:         40
        .size:           8
        .value_kind:     global_buffer
      - .actual_access:  write_only
        .address_space:  global
        .offset:         48
        .size:           8
        .value_kind:     global_buffer
      - .actual_access:  write_only
        .address_space:  global
        .offset:         56
        .size:           8
        .value_kind:     global_buffer
      - .actual_access:  write_only
        .address_space:  global
        .offset:         64
        .size:           8
        .value_kind:     global_buffer
    .group_segment_fixed_size: 9344
    .kernarg_segment_align: 8
    .kernarg_segment_size: 72
    .language:       OpenCL C
    .language_version:
      - 2
      - 0
    .max_flat_workgroup_size: 512
    .name:           _Z14k_scatter_nodePKiS0_PjPiPKfS4_PfS5_PDF16_
    .private_segment_fixed_size: 0
    .sgpr_count:     106
    .sgpr_spill_count: 10
    .symbol:         _Z14k_scatter_nodePKiS0_PjPiPKfS4_PfS5_PDF16_.kd
    .uniform_work_group_size: 1
    .uses_dynamic_stack: false
    .vgpr_count:     118
    .vgpr_spill_count: 0
    .wavefront_size: 64
  - .agpr_count:     0
    .args:
      - .actual_access:  read_only
        .address_space:  global
        .offset:         0
        .size:           8
        .value_kind:     global_buffer
      - .actual_access:  read_only
        .address_space:  global
        .offset:         8
        .size:           8
        .value_kind:     global_buffer
      - .actual_access:  write_only
        .address_space:  global
        .offset:         16
        .size:           8
        .value_kind:     global_buffer
      - .actual_access:  write_only
        .address_space:  global
        .offset:         24
        .size:           8
        .value_kind:     global_buffer
    .group_segment_fixed_size: 3072
    .kernarg_segment_align: 8
    .kernarg_segment_size: 32
    .language:       OpenCL C
    .language_version:
      - 2
      - 0
    .max_flat_workgroup_size: 1024
    .name:           _Z5k_csrPKjPKiPiS3_
    .private_segment_fixed_size: 0
    .sgpr_count:     34
    .sgpr_spill_count: 0
    .symbol:         _Z5k_csrPKjPKiPiS3_.kd
    .uniform_work_group_size: 1
    .uses_dynamic_stack: false
    .vgpr_count:     18
    .vgpr_spill_count: 0
    .wavefront_size: 64
  - .agpr_count:     0
    .args:
      - .actual_access:  read_only
        .address_space:  global
        .offset:         0
        .size:           8
        .value_kind:     global_buffer
      - .actual_access:  read_only
        .address_space:  global
        .offset:         8
        .size:           8
        .value_kind:     global_buffer
      - .actual_access:  read_only
        .address_space:  global
        .offset:         16
        .size:           8
        .value_kind:     global_buffer
      - .actual_access:  read_only
        .address_space:  global
        .offset:         24
        .size:           8
        .value_kind:     global_buffer
      - .actual_access:  read_only
        .address_space:  global
        .offset:         32
        .size:           8
        .value_kind:     global_buffer
      - .actual_access:  read_only
        .address_space:  global
        .offset:         40
        .size:           8
        .value_kind:     global_buffer
      - .actual_access:  read_only
        .address_space:  global
        .offset:         48
        .size:           8
        .value_kind:     global_buffer
      - .actual_access:  read_only
        .address_space:  global
        .offset:         56
        .size:           8
        .value_kind:     global_buffer
      - .actual_access:  read_only
        .address_space:  global
        .offset:         64
        .size:           8
        .value_kind:     global_buffer
      - .actual_access:  read_only
        .address_space:  global
        .offset:         72
        .size:           8
        .value_kind:     global_buffer
      - .actual_access:  write_only
        .address_space:  global
        .offset:         80
        .size:           8
        .value_kind:     global_buffer
      - .actual_access:  write_only
        .address_space:  global
        .offset:         88
        .size:           8
        .value_kind:     global_buffer
      - .actual_access:  write_only
        .address_space:  global
        .offset:         96
        .size:           8
        .value_kind:     global_buffer
      - .offset:         104
        .size:           4
        .value_kind:     hidden_block_count_x
      - .offset:         108
        .size:           4
        .value_kind:     hidden_block_count_y
      - .offset:         112
        .size:           4
        .value_kind:     hidden_block_count_z
      - .offset:         116
        .size:           2
        .value_kind:     hidden_group_size_x
      - .offset:         118
        .size:           2
        .value_kind:     hidden_group_size_y
      - .offset:         120
        .size:           2
        .value_kind:     hidden_group_size_z
      - .offset:         122
        .size:           2
        .value_kind:     hidden_remainder_x
      - .offset:         124
        .size:           2
        .value_kind:     hidden_remainder_y
      - .offset:         126
        .size:           2
        .value_kind:     hidden_remainder_z
      - .offset:         144
        .size:           8
        .value_kind:     hidden_global_offset_x
      - .offset:         152
        .size:           8
        .value_kind:     hidden_global_offset_y
      - .offset:         160
        .size:           8
        .value_kind:     hidden_global_offset_z
      - .offset:         168
        .size:           2
        .value_kind:     hidden_grid_dims
    .group_segment_fixed_size: 54208
    .kernarg_segment_align: 8
    .kernarg_segment_size: 360
    .language:       OpenCL C
    .language_version:
      - 2
      - 0
    .max_flat_workgroup_size: 256
    .name:           _Z8k_layer1PKiS0_PKfS2_PK15HIP_vector_typeIjLj4EEPKDv8_DF16_S9_S2_S2_S2_PDF16_PfSB_
    .private_segment_fixed_size: 0
    .sgpr_count:     106
    .sgpr_spill_count: 7
    .symbol:         _Z8k_layer1PKiS0_PKfS2_PK15HIP_vector_typeIjLj4EEPKDv8_DF16_S9_S2_S2_S2_PDF16_PfSB_.kd
    .uniform_work_group_size: 1
    .uses_dynamic_stack: false
    .vgpr_count:     228
    .vgpr_spill_count: 0
    .wavefront_size: 64
  - .agpr_count:     0
    .args:
      - .actual_access:  read_only
        .address_space:  global
        .offset:         0
        .size:           8
        .value_kind:     global_buffer
      - .actual_access:  read_only
        .address_space:  global
        .offset:         8
        .size:           8
        .value_kind:     global_buffer
      - .actual_access:  read_only
        .address_space:  global
        .offset:         16
        .size:           8
        .value_kind:     global_buffer
      - .actual_access:  read_only
        .address_space:  global
        .offset:         24
        .size:           8
        .value_kind:     global_buffer
      - .actual_access:  read_only
        .address_space:  global
        .offset:         32
        .size:           8
        .value_kind:     global_buffer
      - .actual_access:  read_only
        .address_space:  global
        .offset:         40
        .size:           8
        .value_kind:     global_buffer
      - .actual_access:  write_only
        .address_space:  global
        .offset:         48
        .size:           8
        .value_kind:     global_buffer
    .group_segment_fixed_size: 0
    .kernarg_segment_align: 8
    .kernarg_segment_size: 56
    .language:       OpenCL C
    .language_version:
      - 2
      - 0
    .max_flat_workgroup_size: 256
    .name:           _Z8k_layer2PKiS0_PKfS2_PK15HIP_vector_typeIjLj4EES2_Pf
    .private_segment_fixed_size: 0
    .sgpr_count:     52
    .sgpr_spill_count: 0
    .symbol:         _Z8k_layer2PKiS0_PKfS2_PK15HIP_vector_typeIjLj4EES2_Pf.kd
    .uniform_work_group_size: 1
    .uses_dynamic_stack: false
    .vgpr_count:     70
    .vgpr_spill_count: 0
    .wavefront_size: 64
